# attention softmax: cross-row max/sum reductions in registers with v_permlane16/32_swap instead of ds_bpermute round trips (bit-identical)
# speedup vs baseline: 1.0119x; 1.0083x over previous
; __device__ __forceinline__ unsigned cvt_pk_bf16(float lo, float hi) { unsigned r; asm volatile("v_cvt_pk_bf16_f32 %0, %1, %2" : "=v"(r) : "v"(lo), "v"(hi)); return r; }
; __device__ __forceinline__ void phase_attention(const Frame& F, const Args& a) {
;     ...
;                 if (!isctx) { const int qpos = qpos0 + 16 * m + fr;
; #pragma unroll
;                     for (int nn = 0; nn < 4; ++nn)
; #pragma unroll
;                         for (int j = 0; j < 4; ++j) { const int d = 64 * kt + 16 * nn + 4 * fq + j - qpos; if (d > 128 || d < -128) s[m][nn][j] = -INFINITY; } }
;                 float mx = s[m][0][0];
; #pragma unroll
;                 for (int nn = 0; nn < 4; ++nn)
; #pragma unroll
;                     for (int j = 0; j < 4; ++j) mx = fmaxf(mx, s[m][nn][j]);
;                 mx = fmaxf(mx, __shfl_xor(mx, 16)); mx = fmaxf(mx, __shfl_xor(mx, 32));
;                 const float mnew = fmaxf(mrun[m], mx), alpha = __expf(mrun[m] - mnew); mrun[m] = mnew;
;                 float rs = 0.f;
; #pragma unroll
;                 for (int nn = 0; nn < 4; ++nn)
; #pragma unroll
;                     for (int j = 0; j < 4; ++j) { const float p = __expf(s[m][nn][j] - mnew); s[m][nn][j] = p; rs += p; }
;                 rs += __shfl_xor(rs, 16); rs += __shfl_xor(rs, 32);
;                 lrun[m] = lrun[m] * alpha + rs;
; #pragma unroll
;                 for (int nd = 0; nd < 8; ++nd) o[m][nd] = o[m][nd] * alpha;
; #pragma unroll
;                 for (int ks = 0; ks < 2; ++ks) { u32x4 w; w.x = cvt_pk_bf16(s[m][2 * ks][0], s[m][2 * ks][1]); w.y = cvt_pk_bf16(s[m][2 * ks][2], s[m][2 * ks][3]);
;                     w.z = cvt_pk_bf16(s[m][2 * ks + 1][0], s[m][2 * ks + 1][1]); w.w = cvt_pk_bf16(s[m][2 * ks + 1][2], s[m][2 * ks + 1][3]); pf[m][ks] = __builtin_bit_cast(bf16x8, w); }
.LBB0_2784:
	v_max_f32_e32 v3, v147, v147
	v_max_f32_e32 v201, v146, v146
	v_max_f32_e32 v3, v201, v3
	v_max3_f32 v3, v3, v148, v149
	v_max3_f32 v3, v3, v142, v143
	v_max3_f32 v3, v3, v144, v145
	v_max3_f32 v3, v3, v126, v127
	v_max3_f32 v3, v3, v128, v129
	v_max3_f32 v3, v3, v118, v119
	v_max3_f32 v3, v3, v120, v121
	v_mov_b32_e32 v201, v3
	s_nop 1
	v_permlane16_swap_b32 v201, v3
	s_andn2_b64 vcc, exec, s[16:17]
	s_waitcnt lgkmcnt(0)
	v_max_f32_e32 v201, v201, v201
	v_max_f32_e32 v3, v3, v201
	v_mov_b32_e32 v201, v3
	s_nop 1
	v_permlane32_swap_b32 v201, v3
	s_waitcnt lgkmcnt(0)
	v_max3_f32 v3, v4, v3, v201
	v_sub_f32_e32 v146, v146, v3
	v_sub_f32_e32 v147, v147, v3
	v_mul_f32_e32 v146, 0x3fb8aa3b, v146
	v_sub_f32_e32 v148, v148, v3
	v_sub_f32_e32 v142, v142, v3
	v_mul_f32_e32 v147, 0x3fb8aa3b, v147
	v_exp_f32_e32 v146, v146
	v_sub_f32_e32 v149, v149, v3
	v_mul_f32_e32 v148, 0x3fb8aa3b, v148
	v_exp_f32_e32 v147, v147
	v_mul_f32_e32 v142, 0x3fb8aa3b, v142
	v_mul_f32_e32 v149, 0x3fb8aa3b, v149
	v_exp_f32_e32 v148, v148
	v_exp_f32_e32 v203, v142
	v_sub_f32_e32 v142, v143, v3
	v_exp_f32_e32 v149, v149
	v_mul_f32_e32 v142, 0x3fb8aa3b, v142
	v_add_f32_e32 v201, 0, v146
	v_exp_f32_e32 v204, v142
	v_sub_f32_e32 v142, v144, v3
	v_add_f32_e32 v201, v147, v201
	v_mul_f32_e32 v142, 0x3fb8aa3b, v142
	v_add_f32_e32 v201, v148, v201
	v_exp_f32_e32 v144, v142
	v_sub_f32_e32 v142, v145, v3
	v_sub_f32_e32 v126, v126, v3
	v_add_f32_e32 v201, v149, v201
	v_mul_f32_e32 v142, 0x3fb8aa3b, v142
	v_mul_f32_e32 v126, 0x3fb8aa3b, v126
	v_exp_f32_e32 v145, v142
	v_add_f32_e32 v142, v203, v201
	v_exp_f32_e32 v201, v126
	v_sub_f32_e32 v126, v127, v3
	v_mul_f32_e32 v126, 0x3fb8aa3b, v126
	v_exp_f32_e32 v205, v126
	v_sub_f32_e32 v126, v128, v3
	v_sub_f32_e32 v118, v118, v3
	v_mul_f32_e32 v126, 0x3fb8aa3b, v126
	v_mul_f32_e32 v118, 0x3fb8aa3b, v118
	v_add_f32_e32 v142, v204, v142
	v_exp_f32_e32 v206, v126
	v_sub_f32_e32 v126, v129, v3
	v_exp_f32_e32 v208, v118
	v_sub_f32_e32 v118, v119, v3
	v_add_f32_e32 v142, v144, v142
	v_mul_f32_e32 v126, 0x3fb8aa3b, v126
	v_mul_f32_e32 v118, 0x3fb8aa3b, v118
	v_add_f32_e32 v142, v145, v142
	v_exp_f32_e32 v207, v126
	v_exp_f32_e32 v209, v118
	v_sub_f32_e32 v118, v120, v3
	v_add_f32_e32 v126, v201, v142
	v_mul_f32_e32 v118, 0x3fb8aa3b, v118
	v_add_f32_e32 v126, v205, v126
	v_exp_f32_e32 v210, v118
	v_sub_f32_e32 v118, v121, v3
	v_add_f32_e32 v126, v206, v126
	v_mul_f32_e32 v118, 0x3fb8aa3b, v118
	v_add_f32_e32 v126, v207, v126
	v_exp_f32_e32 v121, v118
	v_add_f32_e32 v118, v208, v126
	v_add_f32_e32 v118, v209, v118
	v_add_f32_e32 v118, v210, v118
	v_add_f32_e32 v118, v121, v118
	v_mov_b32_e32 v119, v118
	s_nop 1
	v_permlane16_swap_b32 v119, v118
	v_cvt_pk_bf16_f32 v126, v146, v147
	v_cvt_pk_bf16_f32 v127, v148, v149
	v_cvt_pk_bf16_f32 v128, v203, v204
	v_cvt_pk_bf16_f32 v129, v144, v145
	s_waitcnt lgkmcnt(0)
	v_add_f32_e32 v142, v118, v119
	v_mov_b32_e32 v143, v142
	s_nop 1
	v_permlane32_swap_b32 v143, v142
	v_cvt_pk_bf16_f32 v118, v201, v205
	v_cvt_pk_bf16_f32 v119, v206, v207
	v_cvt_pk_bf16_f32 v120, v208, v209
	v_cvt_pk_bf16_f32 v121, v210, v121
	s_cbranch_vccnz .LBB0_2786
	v_add_u32_e32 v145, -16, v199
	v_mov_b32_e32 v144, s23
	v_cmp_gt_u32_e32 vcc, s22, v145
	s_nop 1
	v_cndmask_b32_e32 v138, v138, v144, vcc
	v_add_u32_e32 v144, -15, v199
	v_cmp_lt_u32_e32 vcc, s24, v144
	v_add_u32_e32 v144, -14, v199
	s_nop 0
	v_cndmask_b32_e32 v139, v183, v139, vcc
	v_cmp_lt_u32_e32 vcc, s24, v144
	v_add_u32_e32 v144, -13, v199
	s_nop 0
	v_cndmask_b32_e32 v140, v183, v140, vcc
	v_cmp_lt_u32_e32 vcc, s24, v144
	v_mov_b32_e32 v144, s23
	s_nop 0
	v_cndmask_b32_e32 v141, v183, v141, vcc
	v_cmp_gt_u32_e32 vcc, s22, v199
	s_nop 1
	v_cndmask_b32_e32 v134, v134, v144, vcc
	v_cmp_lt_u32_e32 vcc, s24, v200
	s_nop 1
	v_cndmask_b32_e32 v135, v183, v135, vcc
	v_cmp_lt_u32_e32 vcc, s24, v198
	s_nop 1
	v_cndmask_b32_e32 v136, v183, v136, vcc
	v_cmp_lt_u32_e32 vcc, s24, v197
	s_nop 1
	v_cndmask_b32_e32 v137, v183, v137, vcc
	v_cmp_gt_u32_e32 vcc, s22, v196
	s_nop 1
	v_cndmask_b32_e32 v130, v130, v144, vcc
	v_cmp_lt_u32_e32 vcc, s24, v195
	s_nop 1
	v_cndmask_b32_e32 v131, v183, v131, vcc
	v_cmp_lt_u32_e32 vcc, s24, v194
	s_nop 1
	v_cndmask_b32_e32 v132, v183, v132, vcc
	v_cmp_lt_u32_e32 vcc, s24, v193
	s_nop 1
	v_cndmask_b32_e32 v133, v183, v133, vcc
	v_cmp_gt_u32_e32 vcc, s22, v192
	s_nop 1
	v_cndmask_b32_e32 v122, v122, v144, vcc
	v_cmp_lt_u32_e32 vcc, s24, v191
	s_nop 1
	v_cndmask_b32_e32 v123, v183, v123, vcc
	v_cmp_lt_u32_e32 vcc, s24, v190
	s_nop 1
	v_cndmask_b32_e32 v124, v183, v124, vcc
	v_cmp_lt_u32_e32 vcc, s24, v5
	s_nop 1
	v_cndmask_b32_e32 v125, v183, v125, vcc
; __device__ __forceinline__ void phase_attention(const Frame& F, const Args& a) {
;     ...
;                 float mx = s[m][0][0];
; #pragma unroll
;                 for (int nn = 0; nn < 4; ++nn)
; #pragma unroll
;                     for (int j = 0; j < 4; ++j) mx = fmaxf(mx, s[m][nn][j]);
;                 mx = fmaxf(mx, __shfl_xor(mx, 16)); mx = fmaxf(mx, __shfl_xor(mx, 32));
;                 const float mnew = fmaxf(mrun[m], mx), alpha = __expf(mrun[m] - mnew); mrun[m] = mnew;
;                 float rs = 0.f;
; #pragma unroll
;                 for (int nn = 0; nn < 4; ++nn)
; #pragma unroll
;                     for (int j = 0; j < 4; ++j) { const float p = __expf(s[m][nn][j] - mnew); s[m][nn][j] = p; rs += p; }
;                 rs += __shfl_xor(rs, 16); rs += __shfl_xor(rs, 32);
;                 lrun[m] = lrun[m] * alpha + rs;
; #pragma unroll
;                 for (int nd = 0; nd < 8; ++nd) o[m][nd] = o[m][nd] * alpha;
.LBB0_2786:
	s_waitcnt lgkmcnt(0)
	v_add_f32_e32 v5, v142, v143
	v_max_f32_e32 v142, v139, v139
	v_max_f32_e32 v143, v138, v138
	v_max_f32_e32 v142, v143, v142
	v_max3_f32 v142, v142, v140, v141
	v_max3_f32 v142, v142, v134, v135
	v_max3_f32 v142, v142, v136, v137
	v_max3_f32 v142, v142, v130, v131
	v_max3_f32 v142, v142, v132, v133
	v_max3_f32 v142, v142, v122, v123
	v_max3_f32 v142, v142, v124, v125
	v_mov_b32_e32 v143, v142
	s_nop 1
	v_permlane16_swap_b32 v143, v142
	v_sub_f32_e32 v4, v4, v3
	v_mul_f32_e32 v4, 0x3fb8aa3b, v4
	v_exp_f32_e32 v4, v4
	s_add_i32 s0, s39, s42
	s_waitcnt lgkmcnt(0)
	v_max_f32_e32 v143, v143, v143
	v_max_f32_e32 v142, v142, v143
	v_mov_b32_e32 v143, v142
	s_nop 1
	v_permlane32_swap_b32 v143, v142
	v_fmac_f32_e32 v5, v189, v4
	v_pk_mul_f32 v[116:117], v[116:117], v[4:5] op_sel_hi:[1,0]
	v_pk_mul_f32 v[114:115], v[114:115], v[4:5] op_sel_hi:[1,0]
	v_pk_mul_f32 v[112:113], v[112:113], v[4:5] op_sel_hi:[1,0]
	s_waitcnt lgkmcnt(0)
	v_max3_f32 v142, v187, v142, v143
	v_sub_f32_e32 v138, v138, v142
	v_mul_f32_e32 v138, 0x3fb8aa3b, v138
	v_sub_f32_e32 v139, v139, v142
	v_exp_f32_e32 v138, v138
	v_mul_f32_e32 v139, 0x3fb8aa3b, v139
	v_sub_f32_e32 v140, v140, v142
	v_exp_f32_e32 v139, v139
	v_mul_f32_e32 v140, 0x3fb8aa3b, v140
	v_sub_f32_e32 v141, v141, v142
	v_exp_f32_e32 v140, v140
	v_mul_f32_e32 v141, 0x3fb8aa3b, v141
	v_sub_f32_e32 v134, v134, v142
	v_exp_f32_e32 v141, v141
	v_mul_f32_e32 v134, 0x3fb8aa3b, v134
	v_sub_f32_e32 v135, v135, v142
	v_add_f32_e32 v143, 0, v138
	v_exp_f32_e32 v134, v134
	v_mul_f32_e32 v135, 0x3fb8aa3b, v135
	v_sub_f32_e32 v136, v136, v142
	v_sub_f32_e32 v130, v130, v142
	v_add_f32_e32 v143, v139, v143
	v_exp_f32_e32 v135, v135
	v_mul_f32_e32 v136, 0x3fb8aa3b, v136
	v_sub_f32_e32 v137, v137, v142
	v_mul_f32_e32 v130, 0x3fb8aa3b, v130
	v_add_f32_e32 v143, v140, v143
	v_exp_f32_e32 v136, v136
	v_mul_f32_e32 v137, 0x3fb8aa3b, v137
	v_exp_f32_e32 v144, v130
	v_sub_f32_e32 v130, v131, v142
	v_add_f32_e32 v143, v141, v143
	v_exp_f32_e32 v137, v137
	v_mul_f32_e32 v130, 0x3fb8aa3b, v130
	v_add_f32_e32 v143, v134, v143
	v_exp_f32_e32 v145, v130
	v_sub_f32_e32 v130, v132, v142
	v_add_f32_e32 v143, v135, v143
	v_mul_f32_e32 v130, 0x3fb8aa3b, v130
	v_add_f32_e32 v143, v136, v143
	v_exp_f32_e32 v146, v130
	v_sub_f32_e32 v130, v133, v142
	v_sub_f32_e32 v122, v122, v142
	v_add_f32_e32 v143, v137, v143
	v_mul_f32_e32 v130, 0x3fb8aa3b, v130
	v_mul_f32_e32 v122, 0x3fb8aa3b, v122
	v_exp_f32_e32 v147, v130
	v_add_f32_e32 v130, v144, v143
	v_exp_f32_e32 v143, v122
	v_sub_f32_e32 v122, v123, v142
	v_mul_f32_e32 v122, 0x3fb8aa3b, v122
	v_exp_f32_e32 v123, v122
	v_sub_f32_e32 v122, v124, v142
	v_mul_f32_e32 v122, 0x3fb8aa3b, v122
	v_add_f32_e32 v130, v145, v130
	v_exp_f32_e32 v124, v122
	v_sub_f32_e32 v122, v125, v142
	v_add_f32_e32 v130, v146, v130
	v_mul_f32_e32 v122, 0x3fb8aa3b, v122
	v_add_f32_e32 v130, v147, v130
	v_exp_f32_e32 v125, v122
	v_add_f32_e32 v122, v143, v130
	v_add_f32_e32 v122, v123, v122
	v_add_f32_e32 v122, v124, v122
	v_add_f32_e32 v122, v125, v122
	v_mov_b32_e32 v130, v122
	s_nop 1
	v_permlane16_swap_b32 v130, v122
	v_pk_mul_f32 v[110:111], v[110:111], v[4:5] op_sel_hi:[1,0]
	v_pk_mul_f32 v[96:97], v[96:97], v[4:5] op_sel_hi:[1,0]
	v_pk_mul_f32 v[94:95], v[94:95], v[4:5] op_sel_hi:[1,0]
	v_pk_mul_f32 v[100:101], v[100:101], v[4:5] op_sel_hi:[1,0]
	s_waitcnt lgkmcnt(0)
	v_add_f32_e32 v122, v122, v130
	v_pk_mul_f32 v[98:99], v[98:99], v[4:5] op_sel_hi:[1,0]
	v_pk_mul_f32 v[104:105], v[104:105], v[4:5] op_sel_hi:[1,0]
	v_pk_mul_f32 v[102:103], v[102:103], v[4:5] op_sel_hi:[1,0]
	v_pk_mul_f32 v[108:109], v[108:109], v[4:5] op_sel_hi:[1,0]
	v_pk_mul_f32 v[106:107], v[106:107], v[4:5] op_sel_hi:[1,0]
	v_pk_mul_f32 v[88:89], v[88:89], v[4:5] op_sel_hi:[1,0]
	v_pk_mul_f32 v[86:87], v[86:87], v[4:5] op_sel_hi:[1,0]
	v_pk_mul_f32 v[92:93], v[92:93], v[4:5] op_sel_hi:[1,0]
	v_pk_mul_f32 v[90:91], v[90:91], v[4:5] op_sel_hi:[1,0]
	v_sub_f32_e32 v4, v187, v142
	v_mov_b32_e32 v130, v122
	s_nop 1
	v_permlane32_swap_b32 v130, v122
	v_mul_f32_e32 v4, 0x3fb8aa3b, v4
	v_exp_f32_e32 v4, v4
	s_add_i32 s0, s0, s43
	s_waitcnt lgkmcnt(0)
; #define LAS __attribute__((address_space(3)))
; __device__ __forceinline__ unsigned cvt_pk_bf16(float lo, float hi) { unsigned r; asm volatile("v_cvt_pk_bf16_f32 %0, %1, %2" : "=v"(r) : "v"(lo), "v"(hi)); return r; }
; __device__ __forceinline__ void phase_attention(const Frame& F, const Args& a) {
;     ...
;                 rs += __shfl_xor(rs, 16); rs += __shfl_xor(rs, 32);
;                 lrun[m] = lrun[m] * alpha + rs;
; #pragma unroll
;                 for (int nd = 0; nd < 8; ++nd) o[m][nd] = o[m][nd] * alpha;
; #pragma unroll
;                 for (int ks = 0; ks < 2; ++ks) { u32x4 w; w.x = cvt_pk_bf16(s[m][2 * ks][0], s[m][2 * ks][1]); w.y = cvt_pk_bf16(s[m][2 * ks][2], s[m][2 * ks][3]);
;                     w.z = cvt_pk_bf16(s[m][2 * ks + 1][0], s[m][2 * ks + 1][1]); w.w = cvt_pk_bf16(s[m][2 * ks + 1][2], s[m][2 * ks + 1][3]); pf[m][ks] = __builtin_bit_cast(bf16x8, w); }
;             }
;             __builtin_amdgcn_s_setprio(1);
; #pragma unroll
;             for (int ks = 0; ks < 2; ++ks)
; #pragma unroll
;                 for (int nd = 0; nd < 8; ++nd) { const LAS bf16_t* vp = Vs + (16 * nd + fr) * 72 + 32 * ks + 4 * fq;
;                     u32x4 w; const u32x2 lo = *(const LAS u32x2*)vp, hi = *(const LAS u32x2*)(vp + 16); w.x = lo.x; w.y = lo.y; w.z = hi.x; w.w = hi.y;
;                     const bf16x8 vf = __builtin_bit_cast(bf16x8, w);
; #pragma unroll
;                     for (int m = 0; m < 2; ++m) o[m][nd] = __builtin_amdgcn_mfma_f32_16x16x32_bf16(vf, pf[m][ks], o[m][nd], 0, 0, 0); }
;             __builtin_amdgcn_s_setprio(0);
	v_add_f32_e32 v122, v122, v130
	v_fmac_f32_e32 v122, v188, v4
	v_pk_mul_f32 v[72:73], v[72:73], v[4:5] op_sel_hi:[1,0]
	v_pk_mul_f32 v[70:71], v[70:71], v[4:5] op_sel_hi:[1,0]
	v_pk_mul_f32 v[64:65], v[64:65], v[4:5] op_sel_hi:[1,0]
	v_pk_mul_f32 v[62:63], v[62:63], v[4:5] op_sel_hi:[1,0]
	v_pk_mul_f32 v[60:61], v[60:61], v[4:5] op_sel_hi:[1,0]
	v_pk_mul_f32 v[58:59], v[58:59], v[4:5] op_sel_hi:[1,0]
	v_pk_mul_f32 v[56:57], v[56:57], v[4:5] op_sel_hi:[1,0]
	v_pk_mul_f32 v[54:55], v[54:55], v[4:5] op_sel_hi:[1,0]
	v_pk_mul_f32 v[52:53], v[52:53], v[4:5] op_sel_hi:[1,0]
	v_pk_mul_f32 v[50:51], v[50:51], v[4:5] op_sel_hi:[1,0]
	v_pk_mul_f32 v[48:49], v[48:49], v[4:5] op_sel_hi:[1,0]
	v_pk_mul_f32 v[46:47], v[46:47], v[4:5] op_sel_hi:[1,0]
	v_pk_mul_f32 v[44:45], v[44:45], v[4:5] op_sel_hi:[1,0]
	v_pk_mul_f32 v[42:43], v[42:43], v[4:5] op_sel_hi:[1,0]
	v_pk_mul_f32 v[40:41], v[40:41], v[4:5] op_sel_hi:[1,0]
	v_pk_mul_f32 v[38:39], v[38:39], v[4:5] op_sel_hi:[1,0]
	v_cvt_pk_bf16_f32 v130, v138, v139
	v_cvt_pk_bf16_f32 v131, v140, v141
	v_cvt_pk_bf16_f32 v132, v134, v135
	v_cvt_pk_bf16_f32 v133, v136, v137
	v_cvt_pk_bf16_f32 v134, v144, v145
	v_cvt_pk_bf16_f32 v135, v146, v147
	v_cvt_pk_bf16_f32 v136, v143, v123
	v_cvt_pk_bf16_f32 v137, v124, v125
	s_setprio 1
	v_add3_u32 v4, s44, v151, v176
	v_add_u32_e32 v123, 0x4000, v4
	ds_read2_b64 v[138:141], v123 offset0:128 offset1:132
	v_add_u32_e32 v143, 0x4800, v4
	v_add_u32_e32 v144, 0x5000, v4
	v_add_u32_e32 v145, 0x5800, v4
	v_add_u32_e32 v146, 0x6800, v4
	v_add_u32_e32 v147, 0x7000, v4
	v_add_u32_e32 v148, 0x7800, v4
	v_add_u32_e32 v4, 0x8000, v4
	s_waitcnt lgkmcnt(0)
	v_mfma_f32_16x16x32_bf16 v[114:117], v[138:141], v[126:129], v[114:117]
	v_mfma_f32_16x16x32_bf16 v[70:73], v[138:141], v[130:133], v[70:73]
	ds_read2_b64 v[138:141], v143 offset0:160 offset1:164
	s_waitcnt lgkmcnt(0)
	v_mfma_f32_16x16x32_bf16 v[110:113], v[138:141], v[126:129], v[110:113]
	v_mfma_f32_16x16x32_bf16 v[62:65], v[138:141], v[130:133], v[62:65]
	ds_read2_b64 v[138:141], v144 offset0:192 offset1:196
	s_waitcnt lgkmcnt(0)
	v_mfma_f32_16x16x32_bf16 v[94:97], v[138:141], v[126:129], v[94:97]
	v_mfma_f32_16x16x32_bf16 v[58:61], v[138:141], v[130:133], v[58:61]
	ds_read2_b64 v[138:141], v145 offset0:224 offset1:228
	s_waitcnt lgkmcnt(0)
	v_mfma_f32_16x16x32_bf16 v[98:101], v[138:141], v[126:129], v[98:101]
	v_mfma_f32_16x16x32_bf16 v[54:57], v[138:141], v[130:133], v[54:57]
	ds_read2_b64 v[138:141], v146 offset1:4
	s_waitcnt lgkmcnt(0)
	v_mfma_f32_16x16x32_bf16 v[102:105], v[138:141], v[126:129], v[102:105]
	v_mfma_f32_16x16x32_bf16 v[50:53], v[138:141], v[130:133], v[50:53]
	ds_read2_b64 v[138:141], v147 offset0:32 offset1:36
	s_waitcnt lgkmcnt(0)
	v_mfma_f32_16x16x32_bf16 v[106:109], v[138:141], v[126:129], v[106:109]
	v_mfma_f32_16x16x32_bf16 v[46:49], v[138:141], v[130:133], v[46:49]
	ds_read2_b64 v[138:141], v148 offset0:64 offset1:68
	s_waitcnt lgkmcnt(0)
	v_mfma_f32_16x16x32_bf16 v[86:89], v[138:141], v[126:129], v[86:89]
	v_mfma_f32_16x16x32_bf16 v[42:45], v[138:141], v[130:133], v[42:45]
	ds_read2_b64 v[138:141], v4 offset0:96 offset1:100
	s_waitcnt lgkmcnt(0)
	v_mfma_f32_16x16x32_bf16 v[90:93], v[138:141], v[126:129], v[90:93]
	ds_read2_b64 v[124:127], v123 offset0:136 offset1:140
	s_waitcnt lgkmcnt(0)
	v_mfma_f32_16x16x32_bf16 v[114:117], v[124:127], v[118:121], v[114:117]
	v_mfma_f32_16x16x32_bf16 v[70:73], v[124:127], v[134:137], v[70:73]
	ds_read2_b64 v[124:127], v143 offset0:168 offset1:172
	s_waitcnt lgkmcnt(0)
	v_mfma_f32_16x16x32_bf16 v[110:113], v[124:127], v[118:121], v[110:113]
	v_mfma_f32_16x16x32_bf16 v[62:65], v[124:127], v[134:137], v[62:65]
	ds_read2_b64 v[124:127], v144 offset0:200 offset1:204
	s_waitcnt lgkmcnt(0)
	v_mfma_f32_16x16x32_bf16 v[94:97], v[124:127], v[118:121], v[94:97]
	v_mfma_f32_16x16x32_bf16 v[58:61], v[124:127], v[134:137], v[58:61]
	ds_read2_b64 v[124:127], v145 offset0:232 offset1:236
	s_waitcnt lgkmcnt(0)
	v_mfma_f32_16x16x32_bf16 v[98:101], v[124:127], v[118:121], v[98:101]
	v_mfma_f32_16x16x32_bf16 v[54:57], v[124:127], v[134:137], v[54:57]
	ds_read2_b64 v[124:127], v146 offset0:8 offset1:12
	s_waitcnt lgkmcnt(0)
	v_mfma_f32_16x16x32_bf16 v[102:105], v[124:127], v[118:121], v[102:105]
	v_mfma_f32_16x16x32_bf16 v[50:53], v[124:127], v[134:137], v[50:53]
	ds_read2_b64 v[124:127], v147 offset0:40 offset1:44
	s_waitcnt lgkmcnt(0)
	v_mfma_f32_16x16x32_bf16 v[106:109], v[124:127], v[118:121], v[106:109]
	v_mfma_f32_16x16x32_bf16 v[46:49], v[124:127], v[134:137], v[46:49]
	ds_read2_b64 v[124:127], v148 offset0:72 offset1:76
	s_waitcnt lgkmcnt(0)
	v_mfma_f32_16x16x32_bf16 v[86:89], v[124:127], v[118:121], v[86:89]
	v_mfma_f32_16x16x32_bf16 v[42:45], v[124:127], v[134:137], v[42:45]
	ds_read2_b64 v[124:127], v4 offset0:104 offset1:108
	v_mfma_f32_16x16x32_bf16 v[38:41], v[138:141], v[130:133], v[38:41]
	s_waitcnt lgkmcnt(0)
	v_mfma_f32_16x16x32_bf16 v[90:93], v[124:127], v[118:121], v[90:93]
	v_mfma_f32_16x16x32_bf16 v[38:41], v[124:127], v[134:137], v[38:41]
	s_setprio 0
	s_cmp_lg_u32 s0, 0
	s_cbranch_scc0 .LBB0_2791
	s_andn2_b64 vcc, exec, s[14:15]
	s_cbranch_vccnz .LBB0_2789
